# stack18_noprio
# baseline (speedup 1.0000x reference)
_Z6k_rec2PKiS0_S0_PK15HIP_vector_typeIjLj4EEPKfS6_PS2_PS1_IjLj2EEPf:
	s_load_dwordx2 s[6:7], s[0:1], 0x0
	s_load_dwordx2 s[4:5], s[0:1], 0x28
	v_cmp_gt_u32_e32 vcc, 32, v0
	s_and_saveexec_b64 s[8:9], vcc
	v_mov_b32_e32 v1, 0x22000
	v_lshl_or_b32 v1, v0, 2, v1
	v_mov_b32_e32 v2, 0
	ds_write_b32 v1, v2
	s_or_b64 exec, exec, s[8:9]
	v_mov_b32_e32 v3, 0
	v_lshlrev_b32_e32 v2, 2, v0
	s_waitcnt lgkmcnt(0)
	v_lshl_add_u64 v[4:5], s[6:7], 0, v[2:3]
	s_movk_i32 s3, 0x1000
	v_or_b32_e32 v1, 0x400, v0
	v_add_co_u32_e32 v6, vcc, s3, v4
	v_lshlrev_b32_e32 v3, 2, v1
	s_nop 0
	v_addc_co_u32_e32 v7, vcc, 0, v5, vcc
	global_load_dword v68, v2, s[6:7]
	global_load_dword v69, v2, s[6:7] offset:2048
	global_load_dword v70, v3, s[6:7]
	global_load_dword v71, v[6:7], off offset:2048
	v_or_b32_e32 v165, 0x800, v0
	s_movk_i32 s3, 0x2000
	v_lshlrev_b32_e32 v6, 2, v165
	v_add_co_u32_e32 v2, vcc, s3, v4
	v_or_b32_e32 v232, 0xc00, v0
	s_nop 0
	v_addc_co_u32_e32 v3, vcc, 0, v5, vcc
	global_load_dword v72, v6, s[6:7]
	global_load_dword v73, v[2:3], off offset:2048
	v_lshlrev_b32_e32 v2, 2, v232
	global_load_dword v74, v2, s[6:7]
	s_movk_i32 s3, 0x3000
	v_add_co_u32_e32 v2, vcc, s3, v4
	s_ashr_i32 s3, s2, 31
	s_nop 0
	v_addc_co_u32_e32 v3, vcc, 0, v5, vcc
	global_load_dword v75, v[2:3], off offset:2048
	s_lshl_b64 s[6:7], s[2:3], 17
	s_add_u32 s4, s4, s6
	s_addc_u32 s5, s5, s7
	v_mbcnt_lo_u32_b32 v77, -1, 0
	v_mbcnt_hi_u32_b32 v77, -1, v77
	v_and_b32_e32 v83, 64, v77
	v_xor_b32_e32 v84, 32, v77
	v_add_u32_e32 v83, 64, v83
	v_cmp_lt_i32_e32 vcc, v84, v83
	v_xor_b32_e32 v85, 16, v77
	v_xor_b32_e32 v86, 8, v77
	v_cndmask_b32_e32 v84, v77, v84, vcc
	v_lshlrev_b32_e32 v234, 2, v84
	v_cmp_lt_i32_e32 vcc, v85, v83
	v_xor_b32_e32 v87, 4, v77
	v_xor_b32_e32 v88, 2, v77
	v_cndmask_b32_e32 v85, v77, v85, vcc
	v_lshlrev_b32_e32 v235, 2, v85
	v_cmp_lt_i32_e32 vcc, v86, v83
	v_xor_b32_e32 v89, 1, v77
	v_mov_b32_e32 v76, 0x20000
	v_cndmask_b32_e32 v86, v77, v86, vcc
	v_lshlrev_b32_e32 v236, 2, v86
	v_cmp_lt_i32_e32 vcc, v87, v83
	v_lshl_or_b32 v79, v1, 1, v76
	v_lshl_or_b32 v81, v165, 1, v76
	v_cndmask_b32_e32 v87, v77, v87, vcc
	v_cmp_lt_i32_e32 vcc, v88, v83
	v_lshlrev_b32_e32 v237, 2, v87
	v_lshl_or_b32 v76, v232, 1, v76
	v_cndmask_b32_e32 v88, v77, v88, vcc
	v_cmp_lt_i32_e32 vcc, v89, v83
	v_lshlrev_b32_e32 v238, 2, v88
	s_mov_b32 s3, 0
	v_cndmask_b32_e32 v77, v77, v89, vcc
	v_lshlrev_b32_e32 v239, 2, v77
	s_waitcnt vmcnt(7)
	v_lshlrev_b32_e32 v2, 1, v68
	s_waitcnt vmcnt(6)
	v_lshlrev_b32_e32 v4, 1, v69
	v_ashrrev_i32_e32 v3, 31, v2
	v_ashrrev_i32_e32 v5, 31, v4
	v_lshl_add_u64 v[10:11], v[2:3], 4, s[4:5]
	v_lshl_add_u64 v[20:21], v[4:5], 4, s[4:5]
	global_load_dwordx4 v[2:5], v[10:11], off offset:16
	global_load_dwordx4 v[6:9], v[10:11], off
	s_nop 0
	global_load_dwordx4 v[10:13], v[20:21], off offset:16
	global_load_dwordx4 v[14:17], v[20:21], off
	s_waitcnt vmcnt(9)
	v_lshlrev_b32_e32 v18, 1, v70
	v_ashrrev_i32_e32 v19, 31, v18
	v_lshl_add_u64 v[28:29], v[18:19], 4, s[4:5]
	global_load_dwordx4 v[18:21], v[28:29], off offset:16
	global_load_dwordx4 v[22:25], v[28:29], off
	s_waitcnt vmcnt(10)
	v_lshlrev_b32_e32 v26, 1, v71
	v_ashrrev_i32_e32 v27, 31, v26
	v_lshl_add_u64 v[36:37], v[26:27], 4, s[4:5]
	global_load_dwordx4 v[26:29], v[36:37], off offset:16
	global_load_dwordx4 v[30:33], v[36:37], off
	s_waitcnt vmcnt(11)
	v_lshlrev_b32_e32 v34, 1, v72
	v_ashrrev_i32_e32 v35, 31, v34
	v_lshl_add_u64 v[44:45], v[34:35], 4, s[4:5]
	global_load_dwordx4 v[34:37], v[44:45], off offset:16
	global_load_dwordx4 v[38:41], v[44:45], off
	s_waitcnt vmcnt(12)
	v_lshlrev_b32_e32 v42, 1, v73
	v_ashrrev_i32_e32 v43, 31, v42
	v_lshl_add_u64 v[52:53], v[42:43], 4, s[4:5]
	global_load_dwordx4 v[42:45], v[52:53], off offset:16
	global_load_dwordx4 v[46:49], v[52:53], off
	s_waitcnt vmcnt(13)
	v_lshlrev_b32_e32 v50, 1, v74
	v_ashrrev_i32_e32 v51, 31, v50
	v_lshl_add_u64 v[58:59], v[50:51], 4, s[4:5]
	global_load_dwordx4 v[50:53], v[58:59], off offset:16
	global_load_dwordx4 v[54:57], v[58:59], off
	s_waitcnt vmcnt(14)
	v_lshlrev_b32_e32 v58, 1, v75
	v_ashrrev_i32_e32 v59, 31, v58
	v_lshl_add_u64 v[66:67], v[58:59], 4, s[4:5]
	global_load_dwordx4 v[62:65], v[66:67], off
	global_load_dwordx4 v[58:61], v[66:67], off offset:16
	v_lshlrev_b32_e32 v67, 1, v0
	v_or_b32_e32 v233, 0x20000, v67
	s_load_dwordx4 s[8:11], s[0:1], 0x8
	s_load_dwordx2 s[14:15], s[0:1], 0x18
	s_load_dwordx2 s[12:13], s[0:1], 0x40
	s_load_dwordx2 s[6:7], s[0:1], 0x30
	v_or_b32_e32 v78, 0x20400, v67
	v_or_b32_e32 v80, 0x20c00, v67
	ds_write_b16 v233, v68
	ds_write_b16 v78, v69
	ds_write_b16 v79, v70
	ds_write_b16 v80, v71
	v_or_b32_e32 v82, 0x21400, v67
	v_or_b32_e32 v67, 0x21c00, v67
	ds_write_b16 v81, v72
	ds_write_b16 v82, v73
	ds_write_b16 v76, v74
	ds_write_b16 v67, v75
	v_mov_b32_e32 v246, v68
	v_mov_b32_e32 v247, v69
	v_mov_b32_e32 v248, v70
	v_mov_b32_e32 v249, v71
	v_mov_b32_e32 v250, v72
	v_mov_b32_e32 v251, v73
	v_mov_b32_e32 v252, v74
	v_mov_b32_e32 v253, v75
	v_and_b32_e32 v66, 63, v0
	v_cmp_eq_u32_e64 s[4:5], 0, v66
	s_waitcnt lgkmcnt(0)
	s_barrier
	s_waitcnt vmcnt(14)
	v_max3_f32 v84, |v6|, 0, |v7|
	v_max3_f32 v84, v84, |v8|, |v9|
	v_max3_f32 v84, v84, |v2|, |v3|
	v_max3_f32 v84, v84, |v4|, |v5|
	s_waitcnt vmcnt(12)
	v_max3_f32 v84, v84, |v14|, |v15|
	v_max3_f32 v84, v84, |v16|, |v17|
	v_max3_f32 v84, v84, |v10|, |v11|
	v_max3_f32 v84, v84, |v12|, |v13|
	s_waitcnt vmcnt(10)
	v_max3_f32 v84, v84, |v22|, |v23|
	v_max3_f32 v84, v84, |v24|, |v25|
	v_max3_f32 v84, v84, |v18|, |v19|
	v_max3_f32 v84, v84, |v20|, |v21|
	s_waitcnt vmcnt(8)
	v_max3_f32 v84, v84, |v30|, |v31|
	v_max3_f32 v84, v84, |v32|, |v33|
	v_max3_f32 v84, v84, |v26|, |v27|
	v_max3_f32 v84, v84, |v28|, |v29|
	s_waitcnt vmcnt(6)
	v_max3_f32 v84, v84, |v38|, |v39|
	v_max3_f32 v84, v84, |v40|, |v41|
	v_max3_f32 v84, v84, |v34|, |v35|
	v_max3_f32 v84, v84, |v36|, |v37|
	s_waitcnt vmcnt(4)
	v_max3_f32 v84, v84, |v46|, |v47|
	v_max3_f32 v84, v84, |v48|, |v49|
	v_max3_f32 v84, v84, |v42|, |v43|
	v_max3_f32 v84, v84, |v44|, |v45|
	s_waitcnt vmcnt(2)
	v_max3_f32 v84, v84, |v54|, |v55|
	v_max3_f32 v84, v84, |v56|, |v57|
	v_max3_f32 v84, v84, |v50|, |v51|
	v_max3_f32 v84, v84, |v52|, |v53|
	s_waitcnt vmcnt(1)
	v_max3_f32 v84, v84, |v62|, |v63|
	v_max3_f32 v84, v84, |v64|, |v65|
	s_waitcnt vmcnt(0)
	v_max3_f32 v84, v84, |v58|, |v59|
	v_max3_f32 v84, v84, |v60|, |v61|
	ds_bpermute_b32 v90, v234, v84
	s_waitcnt lgkmcnt(0)
	v_max_f32_e32 v85, v90, v90
	v_max_f32_e32 v84, v84, v85
	ds_bpermute_b32 v85, v235, v84
	s_waitcnt lgkmcnt(0)
	v_max_f32_e32 v85, v85, v85
	v_max_f32_e32 v84, v84, v85
	ds_bpermute_b32 v85, v236, v84
	s_waitcnt lgkmcnt(0)
	v_max_f32_e32 v83, v85, v85
	v_max_f32_e32 v83, v84, v83
	ds_bpermute_b32 v84, v237, v83
	s_waitcnt lgkmcnt(0)
	v_max_f32_e32 v68, v84, v84
	v_max_f32_e32 v68, v83, v68
	ds_bpermute_b32 v69, v238, v68
	s_waitcnt lgkmcnt(0)
	v_max_f32_e32 v67, v69, v69
	v_max_f32_e32 v67, v68, v67
	ds_bpermute_b32 v68, v239, v67
	s_and_saveexec_b64 s[16:17], s[4:5]
	s_cbranch_execz .LBB3_7
	s_waitcnt lgkmcnt(0)
	v_max_f32_e32 v68, v68, v68
	v_max_f32_e32 v67, v67, v67
	s_mov_b64 s[18:19], exec
	v_max_f32_e32 v67, v67, v68

.LBB3_36:
	global_load_dwordx4 v[58:61], v[114:115], off
	global_load_dwordx4 v[62:65], v[116:117], off
	global_load_dwordx4 v[66:69], v[118:119], off
	global_load_dwordx4 v[70:73], v[120:121], off
	s_waitcnt lgkmcnt(1)
	v_bfe_u32 v76, v231, 23, 8
	s_cmp_eq_u32 s34, 1
	v_max_u32_e32 v76, 11, v76
	s_cselect_b64 s[24:25], -1, 0
	v_lshlrev_b32_e32 v240, 23, v76
	v_cndmask_b32_e64 v76, 2.0, 1.0, s[24:25]
	s_lshl_b32 s8, s34, 16
	v_mul_f32_e32 v230, v76, v230
	s_and_b32 s67, s8, 0x10000
	v_sub_u32_e32 v164, 0x84000000, v240
	v_pk_fma_f32 v[182:183], v[230:231], v[182:183], v[212:213] op_sel_hi:[0,1,1] neg_lo:[0,0,1] neg_hi:[0,0,1]
	v_pk_fma_f32 v[184:185], v[230:231], v[184:185], v[210:211] op_sel_hi:[0,1,1] neg_lo:[0,0,1] neg_hi:[0,0,1]
	v_pk_fma_f32 v[186:187], v[230:231], v[186:187], v[208:209] op_sel_hi:[0,1,1] neg_lo:[0,0,1] neg_hi:[0,0,1]
	v_pk_fma_f32 v[188:189], v[230:231], v[188:189], v[206:207] op_sel_hi:[0,1,1] neg_lo:[0,0,1] neg_hi:[0,0,1]
	v_fma_mixlo_f16 v78, v182, v164, 0 op_sel_hi:[0,0,0]
	v_fma_mixlo_f16 v79, v184, v164, 0 op_sel_hi:[0,0,0]
	v_fma_mixlo_f16 v80, v186, v164, 0 op_sel_hi:[0,0,0]
	v_fma_mixlo_f16 v81, v188, v164, 0 op_sel_hi:[0,0,0]
	v_lshl_add_u32 v82, v246, 4, s67
	v_fma_mixhi_f16 v78, v183, v164, 0 op_sel_hi:[0,0,0]
	v_fma_mixhi_f16 v79, v185, v164, 0 op_sel_hi:[0,0,0]
	v_fma_mixhi_f16 v80, v187, v164, 0 op_sel_hi:[0,0,0]
	v_fma_mixhi_f16 v81, v189, v164, 0 op_sel_hi:[0,0,0]
	ds_write_b128 v82, v[78:81]
	v_pk_fma_f32 v[198:199], v[230:231], v[198:199], v[196:197] op_sel_hi:[0,1,1] neg_lo:[0,0,1] neg_hi:[0,0,1]
	v_pk_fma_f32 v[200:201], v[230:231], v[200:201], v[194:195] op_sel_hi:[0,1,1] neg_lo:[0,0,1] neg_hi:[0,0,1]
	v_pk_fma_f32 v[202:203], v[230:231], v[202:203], v[192:193] op_sel_hi:[0,1,1] neg_lo:[0,0,1] neg_hi:[0,0,1]
	v_pk_fma_f32 v[204:205], v[230:231], v[204:205], v[190:191] op_sel_hi:[0,1,1] neg_lo:[0,0,1] neg_hi:[0,0,1]
	v_fma_mixlo_f16 v78, v198, v164, 0 op_sel_hi:[0,0,0]
	v_fma_mixlo_f16 v79, v200, v164, 0 op_sel_hi:[0,0,0]
	v_fma_mixlo_f16 v80, v202, v164, 0 op_sel_hi:[0,0,0]
	v_fma_mixlo_f16 v81, v204, v164, 0 op_sel_hi:[0,0,0]
	v_lshl_add_u32 v82, v247, 4, s67
	v_fma_mixhi_f16 v78, v199, v164, 0 op_sel_hi:[0,0,0]
	v_fma_mixhi_f16 v79, v201, v164, 0 op_sel_hi:[0,0,0]
	v_fma_mixhi_f16 v80, v203, v164, 0 op_sel_hi:[0,0,0]
	v_fma_mixhi_f16 v81, v205, v164, 0 op_sel_hi:[0,0,0]
	ds_write_b128 v82, v[78:81]
	v_pk_fma_f32 v[214:215], v[230:231], v[214:215], v[180:181] op_sel_hi:[0,1,1] neg_lo:[0,0,1] neg_hi:[0,0,1]
	v_pk_fma_f32 v[216:217], v[230:231], v[216:217], v[178:179] op_sel_hi:[0,1,1] neg_lo:[0,0,1] neg_hi:[0,0,1]
	v_pk_fma_f32 v[218:219], v[230:231], v[218:219], v[176:177] op_sel_hi:[0,1,1] neg_lo:[0,0,1] neg_hi:[0,0,1]
	v_pk_fma_f32 v[220:221], v[230:231], v[220:221], v[174:175] op_sel_hi:[0,1,1] neg_lo:[0,0,1] neg_hi:[0,0,1]
	v_fma_mixlo_f16 v78, v214, v164, 0 op_sel_hi:[0,0,0]
	v_fma_mixlo_f16 v79, v216, v164, 0 op_sel_hi:[0,0,0]
	v_fma_mixlo_f16 v80, v218, v164, 0 op_sel_hi:[0,0,0]
	v_fma_mixlo_f16 v81, v220, v164, 0 op_sel_hi:[0,0,0]
	v_lshl_add_u32 v82, v248, 4, s67
	v_fma_mixhi_f16 v78, v215, v164, 0 op_sel_hi:[0,0,0]
	v_fma_mixhi_f16 v79, v217, v164, 0 op_sel_hi:[0,0,0]
	v_fma_mixhi_f16 v80, v219, v164, 0 op_sel_hi:[0,0,0]
	v_fma_mixhi_f16 v81, v221, v164, 0 op_sel_hi:[0,0,0]
	ds_write_b128 v82, v[78:81]
	v_pk_fma_f32 v[222:223], v[230:231], v[222:223], v[172:173] op_sel_hi:[0,1,1] neg_lo:[0,0,1] neg_hi:[0,0,1]
	v_pk_fma_f32 v[224:225], v[230:231], v[224:225], v[170:171] op_sel_hi:[0,1,1] neg_lo:[0,0,1] neg_hi:[0,0,1]
	v_pk_fma_f32 v[226:227], v[230:231], v[226:227], v[168:169] op_sel_hi:[0,1,1] neg_lo:[0,0,1] neg_hi:[0,0,1]
	v_pk_fma_f32 v[228:229], v[230:231], v[228:229], v[166:167] op_sel_hi:[0,1,1] neg_lo:[0,0,1] neg_hi:[0,0,1]
	v_fma_mixlo_f16 v78, v222, v164, 0 op_sel_hi:[0,0,0]
	v_fma_mixlo_f16 v79, v224, v164, 0 op_sel_hi:[0,0,0]
	v_fma_mixlo_f16 v80, v226, v164, 0 op_sel_hi:[0,0,0]
	v_fma_mixlo_f16 v81, v228, v164, 0 op_sel_hi:[0,0,0]
	v_lshl_add_u32 v82, v249, 4, s67
	v_fma_mixhi_f16 v78, v223, v164, 0 op_sel_hi:[0,0,0]
	v_fma_mixhi_f16 v79, v225, v164, 0 op_sel_hi:[0,0,0]
	v_fma_mixhi_f16 v80, v227, v164, 0 op_sel_hi:[0,0,0]
	v_fma_mixhi_f16 v81, v229, v164, 0 op_sel_hi:[0,0,0]
	v_pk_mul_f32 v[206:207], v[38:39], v[74:75]
	v_pk_mul_f32 v[208:209], v[40:41], v[74:75]
	v_pk_mul_f32 v[210:211], v[34:35], v[74:75]
	v_pk_mul_f32 v[212:213], v[36:37], v[74:75]
	v_pk_mul_f32 v[190:191], v[46:47], v[74:75]
	v_pk_mul_f32 v[192:193], v[48:49], v[74:75]
	v_pk_mul_f32 v[194:195], v[42:43], v[74:75]
	v_pk_mul_f32 v[196:197], v[44:45], v[74:75]
	v_pk_mul_f32 v[174:175], v[54:55], v[74:75]
	v_pk_mul_f32 v[176:177], v[56:57], v[74:75]
	v_pk_mul_f32 v[178:179], v[50:51], v[74:75]
	v_pk_mul_f32 v[180:181], v[52:53], v[74:75]
	v_pk_mul_f32 v[166:167], v[124:125], v[74:75]
	v_pk_mul_f32 v[168:169], v[128:129], v[74:75]
	v_pk_mul_f32 v[170:171], v[126:127], v[74:75]
	v_pk_mul_f32 v[172:173], v[130:131], v[74:75]
	s_andn2_b64 vcc, exec, s[12:13]
	s_mov_b64 s[24:25], -1
	ds_write_b128 v82, v[78:81]
	s_cbranch_vccnz .LBB3_38
	s_mov_b64 s[24:25], 0
